# fp8 GEMM prologues: removed the compiler's vmcnt(0) after each of the NST dummy stores (78 serialized system-scope store round trips) and made them plain; + down epilogue wait fix + final RMSNorm rewr
# speedup vs baseline: 1.0126x; 1.0126x over previous
.LBB0_1535:
	s_add_u32 s16, s8, 0x4fc00000
	s_addc_u32 s17, s9, 0
	s_lshl_b32 s18, s18, 12
	s_lshl_b32 s24, s19, 13
	s_and_b32 s25, s18, 0x3000
	s_mov_b64 s[18:19], 0x80
	s_add_i32 m0, s57, 0x18000
	v_lshl_add_u64 v[6:7], v[6:7], 0, s[18:19]
	s_waitcnt vmcnt(2)
	s_barrier
	global_load_lds_dwordx4 v[6:7], off
	s_add_i32 m0, s57, 0x1a000
	s_add_u32 s20, s8, 0x67c00080
	v_lshl_add_u64 v[4:5], v[4:5], 0, s[18:19]
	s_addc_u32 s21, s9, 0
	s_add_i32 s61, s57, 0x8000
	s_add_i32 s62, s57, 0xa000
	global_load_lds_dwordx4 v[4:5], off
	v_lshl_add_u64 v[4:5], s[20:21], 0, v[142:143]
	s_mov_b32 m0, s61
	s_add_u32 s22, s82, 0x8080
	global_load_lds_dwordx4 v[4:5], off
	v_lshl_add_u64 v[4:5], s[20:21], 0, v[154:155]
	s_mov_b32 m0, s62
	s_addc_u32 s23, s83, 0
	global_load_lds_dwordx4 v[4:5], off
	s_add_i32 m0, s57, 0x1c000
	v_lshl_add_u64 v[4:5], s[22:23], 0, v[138:139]
	global_load_lds_dwordx4 v[4:5], off
	v_lshl_add_u64 v[4:5], s[22:23], 0, v[140:141]
	s_add_i32 m0, s57, 0x1e000
	s_add_i32 s63, s57, 0xc000
	global_load_lds_dwordx4 v[4:5], off
	v_lshl_add_u64 v[4:5], s[20:21], 0, v[152:153]
	s_mov_b32 m0, s63
	s_add_i32 s64, s57, 0xe000
	global_load_lds_dwordx4 v[4:5], off
	v_lshl_add_u64 v[4:5], s[20:21], 0, v[150:151]
	s_mov_b32 m0, s64
	v_readlane_b32 s22, v254, 17
	global_load_lds_dwordx4 v[4:5], off
	v_and_b32_e32 v4, 15, v2
	v_and_b32_e32 v5, 48, v2
	v_lshlrev_b32_e32 v4, 6, v4
	v_lshlrev_b32_e32 v7, 2, v2
	v_readlane_b32 s23, v254, 18
	s_add_u32 s22, s8, s22
	v_or_b32_e32 v6, v4, v5
	v_and_b32_e32 v7, 32, v7
	s_addc_u32 s23, s9, s23
	v_bitop3_b32 v4, v4, v7, v5 bitop3:0x36
	v_bitop3_b32 v5, v6, s24, v7 bitop3:0xde
	s_mov_b32 s24, 0
	v_lshl_add_u64 v[2:3], v[2:3], 4, s[22:23]
	s_mov_b32 s22, 0x72600000
	v_or_b32_e32 v163, s25, v4
	v_add_co_u32_e32 v2, vcc, s22, v2
	s_mov_b32 s25, s24
	s_add_u32 s22, s8, 0x67c00100
	s_mov_b32 s26, s24
	s_mov_b32 s27, s24
	v_mov_b64_e32 v[6:7], s[24:25]
	s_addc_u32 s23, s9, 0
	v_mov_b64_e32 v[8:9], s[26:27]
	s_add_u32 s24, s8, 0x67c00180
	s_addc_u32 s25, s9, 0
	s_cmpk_lt_u32 s7, 0x100
	s_cselect_b64 s[26:27], -1, 0
	s_add_u32 s28, s8, 0x67c00200
	s_addc_u32 s29, s9, 0
	s_add_u32 s30, s8, 0x67c00280
	s_addc_u32 s31, s9, 0
	s_add_u32 s34, s8, 0x67c00300
	s_addc_u32 s35, s9, 0
	v_addc_co_u32_e32 v3, vcc, 0, v3, vcc
	s_add_u32 s36, s8, 0x67c00380
	global_store_dwordx4 v[2:3], v[6:9], off
	global_store_dwordx4 v[2:3], v[6:9], off
	global_store_dwordx4 v[2:3], v[6:9], off
	global_store_dwordx4 v[2:3], v[6:9], off
	s_addc_u32 s37, s9, 0
	s_ashr_i32 s65, s95, 31
	s_ashr_i32 s7, s6, 31
	s_waitcnt vmcnt(12)
	s_add_u32 s38, s2, s95
	s_addc_u32 s39, s96, s65
	s_add_i32 s66, 0, 0x10000
	s_add_i32 s67, 0, 0x14000
	v_add_u32_e32 v164, 0, v5
	v_mov_b64_e32 v[144:145], s[6:7]
	v_add_u32_e32 v165, s66, v163
	v_add_u32_e32 v166, s67, v163
	s_mov_b64 s[40:41], 0x100
	s_mov_b64 s[42:43], 0x180
	s_mov_b64 s[44:45], 0x200
	s_mov_b64 s[46:47], 0x280
	s_mov_b64 s[48:49], 0x300
	s_mov_b64 s[50:51], 0x380
	s_mov_b32 s70, 0xc0c00000
	v_mov_b32_e32 v167, 0x41000000
	s_barrier
	s_branch .LBB0_1538

.LBB0_1614:
	s_add_u32 s16, s10, 0x2ec00000
	s_addc_u32 s17, s11, 0
	s_lshl_b32 s9, s18, 13
	s_lshl_b32 s18, s19, 12
	s_and_b32 s21, s18, 0x3000
	s_mov_b64 s[18:19], 0x80
	s_add_i32 m0, s49, 0x18000
	v_lshl_add_u64 v[18:19], v[18:19], 0, s[18:19]
	s_waitcnt vmcnt(2)
	s_barrier
	global_load_lds_dwordx4 v[18:19], off
	v_lshl_add_u64 v[16:17], v[16:17], 0, s[18:19]
	s_add_i32 m0, s49, 0x1a000
	s_add_i32 s61, s49, 0x8000
	s_add_i32 s62, s49, 0xa000
	global_load_lds_dwordx4 v[16:17], off
	v_lshl_add_u64 v[12:13], v[12:13], 0, s[18:19]
	s_mov_b32 m0, s61
	s_add_u32 s22, s72, 0x8080
	global_load_lds_dwordx4 v[12:13], off
	v_lshl_add_u64 v[12:13], v[14:15], 0, s[18:19]
	s_mov_b32 m0, s62
	s_addc_u32 s23, s73, 0
	global_load_lds_dwordx4 v[12:13], off
	s_add_i32 m0, s49, 0x1c000
	v_lshl_add_u64 v[12:13], s[22:23], 0, v[140:141]
	global_load_lds_dwordx4 v[12:13], off
	s_add_i32 m0, s49, 0x1e000
	v_lshl_add_u64 v[12:13], s[22:23], 0, v[144:145]
	s_add_u32 s22, s68, 0x20080
	s_addc_u32 s23, s69, 0
	s_add_i32 s63, s49, 0xc000
	global_load_lds_dwordx4 v[12:13], off
	v_lshl_add_u64 v[12:13], s[22:23], 0, v[138:139]
	s_mov_b32 m0, s63
	s_add_i32 s64, s49, 0xe000
	global_load_lds_dwordx4 v[12:13], off
	v_lshl_add_u64 v[12:13], s[22:23], 0, v[142:143]
	s_mov_b32 m0, s64
	v_readlane_b32 s22, v254, 17
	global_load_lds_dwordx4 v[12:13], off
	v_and_b32_e32 v12, 15, v10
	v_and_b32_e32 v13, 48, v10
	v_lshlrev_b32_e32 v12, 6, v12
	v_lshlrev_b32_e32 v15, 2, v10
	v_readlane_b32 s23, v254, 18
	s_add_u32 s10, s10, s22
	v_or_b32_e32 v14, v12, v13
	v_and_b32_e32 v15, 32, v15
	s_addc_u32 s11, s11, s23
	v_bitop3_b32 v12, v12, v15, v13 bitop3:0x36
	v_bitop3_b32 v13, v14, s9, v15 bitop3:0xde
	v_lshl_add_u64 v[10:11], v[10:11], 4, s[10:11]
	s_mov_b32 s9, 0x72600000
	s_mov_b32 s10, s8
	s_mov_b32 s11, s8
	v_add_co_u32_e32 v10, vcc, s9, v10
	s_mov_b32 s9, s8
	v_mov_b64_e32 v[16:17], s[10:11]
	v_addc_co_u32_e32 v11, vcc, 0, v11, vcc
	v_mov_b64_e32 v[14:15], s[8:9]
	s_cmpk_lt_u32 s20, 0x100
	global_store_dwordx4 v[10:11], v[14:17], off
	global_store_dwordx4 v[10:11], v[14:17], off
	global_store_dwordx4 v[10:11], v[14:17], off
	global_store_dwordx4 v[10:11], v[14:17], off
	global_store_dwordx4 v[10:11], v[14:17], off
	global_store_dwordx4 v[10:11], v[14:17], off
	global_store_dwordx4 v[10:11], v[14:17], off
	global_store_dwordx4 v[10:11], v[14:17], off
	s_cselect_b64 s[10:11], -1, 0
	s_ashr_i32 s65, s95, 31
	s_waitcnt vmcnt(16)
	s_add_u32 s20, s2, s95
	v_or_b32_e32 v160, s21, v12
	s_addc_u32 s21, s96, s65
	s_add_i32 s66, 0, 0x10000
	s_add_i32 s67, 0, 0x14000
	v_add_u32_e32 v161, 0, v13
	v_mov_b64_e32 v[148:149], s[6:7]
	v_add_u32_e32 v162, s66, v160
	v_add_u32_e32 v163, s67, v160
	s_mov_b64 s[22:23], 0x100
	s_mov_b64 s[24:25], 0x180
	s_mov_b64 s[26:27], 0x200
	s_mov_b64 s[28:29], 0x280
	s_mov_b64 s[30:31], 0x300
	s_mov_b64 s[34:35], 0x380
	s_mov_b32 s36, 0x3cd083aa
	s_mov_b32 s70, 0xc3e00000
	v_mov_b32_e32 v164, 0x43e00000
	s_barrier
	s_branch .LBB0_1617

.LBB0_1767:
	s_add_u32 s41, s20, 0x4fc00000
	s_addc_u32 s43, s21, 0
	s_add_u32 s54, s20, 0x5fc00000
	s_addc_u32 s55, s21, 0
	s_add_u32 s56, s20, 0x26c00000
	s_addc_u32 s57, s21, 0
	s_add_u32 s58, s20, 0x71400000
	s_addc_u32 s59, s21, 0
	s_add_u32 s16, s20, 0x57c00000
	s_mov_b64 s[18:19], 0x80
	s_addc_u32 s17, s21, 0
	s_lshl_b32 s10, s10, 12
	s_add_i32 m0, s6, 0x18000
	v_lshl_add_u64 v[26:27], v[26:27], 0, s[18:19]
	s_lshl_b32 s9, s9, 13
	s_and_b32 s23, s10, 0x3000
	s_waitcnt vmcnt(2)
	s_barrier
	global_load_lds_dwordx4 v[26:27], off
	v_lshl_add_u64 v[24:25], v[24:25], 0, s[18:19]
	s_add_i32 m0, s6, 0x1a000
	s_add_i32 s60, s6, 0x8000
	s_add_i32 s61, s6, 0xa000
	global_load_lds_dwordx4 v[24:25], off
	v_lshl_add_u64 v[20:21], v[20:21], 0, s[18:19]
	s_mov_b32 m0, s60
	s_add_u32 s10, s78, 0x8080
	global_load_lds_dwordx4 v[20:21], off
	v_lshl_add_u64 v[20:21], v[22:23], 0, s[18:19]
	s_mov_b32 m0, s61
	s_addc_u32 s11, s79, 0
	global_load_lds_dwordx4 v[20:21], off
	s_add_i32 m0, s6, 0x1c000
	v_lshl_add_u64 v[20:21], s[10:11], 0, v[168:169]
	global_load_lds_dwordx4 v[20:21], off
	s_add_i32 m0, s6, 0x1e000
	v_lshl_add_u64 v[20:21], s[10:11], 0, v[172:173]
	s_add_u32 s10, s74, 0x20080
	s_addc_u32 s11, s75, 0
	s_add_i32 s62, s6, 0xc000
	global_load_lds_dwordx4 v[20:21], off
	v_lshl_add_u64 v[20:21], s[10:11], 0, v[166:167]
	s_mov_b32 m0, s62
	s_add_i32 s63, s6, 0xe000
	global_load_lds_dwordx4 v[20:21], off
	v_lshl_add_u64 v[20:21], s[10:11], 0, v[170:171]
	s_mov_b32 m0, s63
	v_and_b32_e32 v1, 15, v18
	global_load_lds_dwordx4 v[20:21], off
	v_readlane_b32 s10, v254, 17
	v_and_b32_e32 v20, 48, v18
	v_lshlrev_b32_e32 v1, 6, v1
	v_lshlrev_b32_e32 v22, 2, v18
	v_readlane_b32 s11, v254, 18
	s_add_u32 s10, s20, s10
	v_or_b32_e32 v21, v1, v20
	v_and_b32_e32 v22, 32, v22
	s_addc_u32 s11, s21, s11
	v_bitop3_b32 v1, v1, v22, v20 bitop3:0x36
	v_bitop3_b32 v20, v21, s9, v22 bitop3:0xde
	v_lshl_add_u64 v[18:19], v[18:19], 4, s[10:11]
	s_mov_b32 s9, 0x72600000
	s_mov_b32 s10, s8
	s_mov_b32 s11, s8
	v_add_co_u32_e32 v18, vcc, s9, v18
	s_mov_b32 s9, s8
	v_mov_b64_e32 v[24:25], s[10:11]
	v_addc_co_u32_e32 v19, vcc, 0, v19, vcc
	v_mov_b64_e32 v[22:23], s[8:9]
	global_store_dwordx4 v[18:19], v[22:25], off
	global_store_dwordx4 v[18:19], v[22:25], off
	global_store_dwordx4 v[18:19], v[22:25], off
	global_store_dwordx4 v[18:19], v[22:25], off
	global_store_dwordx4 v[18:19], v[22:25], off
	global_store_dwordx4 v[18:19], v[22:25], off
	global_store_dwordx4 v[18:19], v[22:25], off
	global_store_dwordx4 v[18:19], v[22:25], off
	global_store_dwordx4 v[18:19], v[22:25], off
	global_store_dwordx4 v[18:19], v[22:25], off
	global_store_dwordx4 v[18:19], v[22:25], off
	global_store_dwordx4 v[18:19], v[22:25], off
	global_store_dwordx4 v[18:19], v[22:25], off
	global_store_dwordx4 v[18:19], v[22:25], off
	global_store_dwordx4 v[18:19], v[22:25], off
	global_store_dwordx4 v[18:19], v[22:25], off
	global_store_dwordx4 v[18:19], v[22:25], off
	global_store_dwordx4 v[18:19], v[22:25], off
	s_cmpk_lt_u32 s22, 0x100
	s_waitcnt vmcnt(26)
	s_cselect_b64 s[20:21], -1, 0
	s_ashr_i32 s65, s95, 31
	s_add_u32 s22, s2, s95
	v_or_b32_e32 v1, s23, v1
	v_add_u32_e32 v203, 0, v20
	s_addc_u32 s23, s96, s65
	s_add_i32 s66, 0, 0x10000
	s_add_i32 s67, 0, 0x14000
	s_mov_b64 s[24:25], 0x100
	s_mov_b64 s[26:27], 0x180
	s_mov_b64 s[28:29], 0x200
	s_mov_b64 s[30:31], 0x280
	s_mov_b64 s[34:35], 0x300
	s_mov_b64 s[36:37], 0x380
	s_mov_b32 s38, 0x3d800000
	s_mov_b32 s40, 0xbfb8aa3b
	s_mov_b32 s42, 0x3e000000
	v_mov_b64_e32 v[176:177], 0x400
	v_mov_b64_e32 v[178:179], 0x3ff
	s_barrier
	s_branch .LBB0_1770

.LBB0_2289:
	s_add_u32 s37, s10, 0x26c00000
	s_addc_u32 s54, s11, 0
	s_add_u32 s55, s10, 0x1ec00000
	s_addc_u32 s56, s11, 0
	s_add_u32 s58, s10, 0x71800000
	s_addc_u32 s59, s11, 0
	s_add_u32 s60, s10, 0x67c00000
	s_addc_u32 s61, s11, 0
	v_readlane_b32 s20, v254, 17
	v_readlane_b32 s21, v254, 18
	s_add_u32 s10, s10, s20
	s_addc_u32 s11, s11, s21
	s_lshl_b32 s19, s16, 13
	s_mov_b64 s[16:17], 0x80
	s_lshl_b32 s9, s9, 12
	s_add_i32 m0, s6, 0x18000
	v_lshl_add_u64 v[10:11], v[10:11], 0, s[16:17]
	s_and_b32 s9, s9, 0x3000
	s_waitcnt vmcnt(2)
	s_barrier
	global_load_lds_dwordx4 v[10:11], off
	v_lshl_add_u64 v[8:9], v[8:9], 0, s[16:17]
	s_add_i32 m0, s6, 0x1a000
	s_add_i32 s62, s6, 0x8000
	s_add_i32 s63, s6, 0xa000
	global_load_lds_dwordx4 v[8:9], off
	v_lshl_add_u64 v[4:5], v[4:5], 0, s[16:17]
	s_mov_b32 m0, s62
	s_add_u32 s20, s70, 0x8080
	global_load_lds_dwordx4 v[4:5], off
	v_lshl_add_u64 v[4:5], v[6:7], 0, s[16:17]
	s_mov_b32 m0, s63
	s_addc_u32 s21, s71, 0
	global_load_lds_dwordx4 v[4:5], off
	s_add_i32 m0, s6, 0x1c000
	v_lshl_add_u64 v[4:5], s[20:21], 0, v[134:135]
	global_load_lds_dwordx4 v[4:5], off
	s_add_i32 m0, s6, 0x1e000
	v_lshl_add_u64 v[4:5], s[20:21], 0, v[130:131]
	s_add_u32 s20, s48, 0x20080
	s_addc_u32 s21, s49, 0
	s_add_i32 s64, s6, 0xc000
	global_load_lds_dwordx4 v[4:5], off
	v_lshl_add_u64 v[4:5], s[20:21], 0, v[136:137]
	s_mov_b32 m0, s64
	s_add_i32 s65, s6, 0xe000
	global_load_lds_dwordx4 v[4:5], off
	v_lshl_add_u64 v[4:5], s[20:21], 0, v[132:133]
	s_mov_b32 m0, s65
	v_and_b32_e32 v1, 15, v2
	global_load_lds_dwordx4 v[4:5], off
	v_lshlrev_b32_e32 v6, 2, v2
	v_and_b32_e32 v4, 48, v2
	v_lshlrev_b32_e32 v1, 6, v1
	v_and_b32_e32 v6, 32, v6
	v_or_b32_e32 v5, v1, v4
	v_bitop3_b32 v1, v1, v6, v4 bitop3:0x36
	v_or_b32_e32 v1, s9, v1
	v_lshl_add_u64 v[2:3], v[2:3], 4, s[10:11]
	s_mov_b32 s9, 0x72600000
	v_add_co_u32_e32 v2, vcc, s9, v2
	s_mov_b32 s9, s8
	v_bitop3_b32 v4, v5, s19, v6 bitop3:0xde
	s_mov_b32 s10, s8
	s_mov_b32 s11, s8
	v_mov_b64_e32 v[6:7], s[8:9]
	v_addc_co_u32_e32 v3, vcc, 0, v3, vcc
	v_mov_b64_e32 v[8:9], s[10:11]
	global_store_dwordx4 v[2:3], v[6:9], off
	global_store_dwordx4 v[2:3], v[6:9], off
	global_store_dwordx4 v[2:3], v[6:9], off
	global_store_dwordx4 v[2:3], v[6:9], off
	global_store_dwordx4 v[2:3], v[6:9], off
	global_store_dwordx4 v[2:3], v[6:9], off
	global_store_dwordx4 v[2:3], v[6:9], off
	global_store_dwordx4 v[2:3], v[6:9], off
	global_store_dwordx4 v[2:3], v[6:9], off
	global_store_dwordx4 v[2:3], v[6:9], off
	global_store_dwordx4 v[2:3], v[6:9], off
	global_store_dwordx4 v[2:3], v[6:9], off
	global_store_dwordx4 v[2:3], v[6:9], off
	global_store_dwordx4 v[2:3], v[6:9], off
	global_store_dwordx4 v[2:3], v[6:9], off
	global_store_dwordx4 v[2:3], v[6:9], off
	global_store_dwordx4 v[2:3], v[6:9], off
	global_store_dwordx4 v[2:3], v[6:9], off
	s_cmpk_lt_u32 s18, 0x100
	s_waitcnt vmcnt(26)
	s_cselect_b64 s[18:19], -1, 0
	s_add_u32 s20, s2, s97
	s_addc_u32 s21, s96, s57
	s_add_i32 s66, 0, 0x10000
	s_add_i32 s67, 0, 0x14000
	v_add_u32_e32 v160, 0, v4
	v_mov_b64_e32 v[140:141], 0x400
	v_mov_b64_e32 v[142:143], 0x3ff
	v_add_u32_e32 v161, s66, v1
	v_add_u32_e32 v162, s67, v1
	s_mov_b64 s[22:23], 0x100
	s_mov_b64 s[24:25], 0x180
	s_mov_b64 s[26:27], 0x200
	s_mov_b64 s[28:29], 0x280
	s_mov_b64 s[30:31], 0x300
	s_mov_b64 s[34:35], 0x380
	s_mov_b32 s36, 0x3d800000
	s_mov_b32 s69, 0xc3e00000
	v_mov_b32_e32 v163, 0x43e00000
	s_barrier
	s_branch .LBB0_2292

.LBB0_3337:
	s_add_u32 s18, s10, 0x4fc00000
	s_addc_u32 s19, s11, 0
	s_lshl_b32 s20, s20, 12
	s_lshl_b32 s26, s21, 13
	s_and_b32 s27, s20, 0x3000
	s_mov_b64 s[20:21], 0x80
	s_add_i32 m0, s55, 0x18000
	v_lshl_add_u64 v[6:7], v[6:7], 0, s[20:21]
	s_waitcnt vmcnt(2)
	s_barrier
	global_load_lds_dwordx4 v[6:7], off
	s_add_i32 m0, s55, 0x1a000
	s_add_u32 s22, s10, 0x67c00080
	v_lshl_add_u64 v[4:5], v[4:5], 0, s[20:21]
	s_addc_u32 s23, s11, 0
	s_add_i32 s59, s55, 0x8000
	s_add_i32 s60, s55, 0xa000
	global_load_lds_dwordx4 v[4:5], off
	v_lshl_add_u64 v[4:5], s[22:23], 0, v[142:143]
	s_mov_b32 m0, s59
	s_add_u32 s24, s78, 0x8080
	global_load_lds_dwordx4 v[4:5], off
	v_lshl_add_u64 v[4:5], s[22:23], 0, v[154:155]
	s_mov_b32 m0, s60
	s_addc_u32 s25, s79, 0
	global_load_lds_dwordx4 v[4:5], off
	s_add_i32 m0, s55, 0x1c000
	v_lshl_add_u64 v[4:5], s[24:25], 0, v[138:139]
	global_load_lds_dwordx4 v[4:5], off
	v_lshl_add_u64 v[4:5], s[24:25], 0, v[140:141]
	s_add_i32 m0, s55, 0x1e000
	s_add_i32 s61, s55, 0xc000
	global_load_lds_dwordx4 v[4:5], off
	v_lshl_add_u64 v[4:5], s[22:23], 0, v[152:153]
	s_mov_b32 m0, s61
	s_add_i32 s69, s55, 0xe000
	global_load_lds_dwordx4 v[4:5], off
	v_lshl_add_u64 v[4:5], s[22:23], 0, v[150:151]
	s_mov_b32 m0, s69
	v_lshlrev_b32_e32 v7, 2, v2
	global_load_lds_dwordx4 v[4:5], off
	v_and_b32_e32 v4, 15, v2
	v_and_b32_e32 v5, 48, v2
	v_lshlrev_b32_e32 v4, 6, v4
	v_and_b32_e32 v7, 32, v7
	v_or_b32_e32 v6, v4, v5
	v_bitop3_b32 v4, v4, v7, v5 bitop3:0x36
	v_bitop3_b32 v5, v6, s26, v7 bitop3:0xde
	v_or_b32_e32 v165, s27, v4
	v_readlane_b32 s26, v254, 17
	v_readlane_b32 s27, v254, 18
	s_add_u32 s26, s10, s26
	s_addc_u32 s27, s11, s27
	s_mov_b32 s24, 0
	v_lshl_add_u64 v[2:3], v[2:3], 4, s[26:27]
	s_mov_b32 s25, 0x72600000
	v_add_co_u32_e32 v2, vcc, s25, v2
	s_mov_b32 s25, s24
	s_mov_b32 s26, s24
	s_mov_b32 s27, s24
	v_mov_b64_e32 v[6:7], s[24:25]
	v_mov_b64_e32 v[8:9], s[26:27]
	s_add_u32 s24, s10, 0x67c00100
	s_addc_u32 s25, s11, 0
	s_add_u32 s26, s10, 0x67c00180
	s_addc_u32 s27, s11, 0
	s_cmpk_lt_u32 s9, 0x100
	s_cselect_b64 s[28:29], -1, 0
	s_add_u32 s30, s10, 0x67c00200
	s_addc_u32 s31, s11, 0
	s_add_u32 s34, s10, 0x67c00280
	s_addc_u32 s35, s11, 0
	s_add_u32 s36, s10, 0x67c00300
	s_addc_u32 s37, s11, 0
	v_addc_co_u32_e32 v3, vcc, 0, v3, vcc
	s_add_u32 s38, s10, 0x67c00380
	global_store_dwordx4 v[2:3], v[6:9], off
	global_store_dwordx4 v[2:3], v[6:9], off
	global_store_dwordx4 v[2:3], v[6:9], off
	global_store_dwordx4 v[2:3], v[6:9], off
	s_addc_u32 s39, s11, 0
	s_ashr_i32 s75, s95, 31
	s_ashr_i32 s9, s8, 31
	s_waitcnt vmcnt(12)
	s_add_u32 s40, s2, s95
	s_addc_u32 s41, s96, s75
	s_add_i32 s77, 0, 0x10000
	s_add_i32 s80, 0, 0x14000
	v_add_u32_e32 v166, 0, v5
	v_mov_b64_e32 v[144:145], s[8:9]
	v_add_u32_e32 v167, s77, v165
	v_add_u32_e32 v168, s80, v165
	s_mov_b64 s[42:43], 0x100
	s_mov_b64 s[44:45], 0x180
	s_mov_b64 s[46:47], 0x200
	s_mov_b64 s[48:49], 0x280
	s_mov_b64 s[50:51], 0x300
	s_mov_b64 s[62:63], 0x380
	s_mov_b32 s81, 0xc0c00000
	v_mov_b32_e32 v170, 0x41000000
	s_barrier
	s_branch .LBB0_3340

.LBB0_3416:
	s_add_u32 s16, s10, 0x2ec00000
	s_addc_u32 s17, s11, 0
	s_lshl_b32 s9, s18, 13
	s_lshl_b32 s18, s19, 12
	s_and_b32 s21, s18, 0x3000
	s_mov_b64 s[18:19], 0x80
	s_add_i32 m0, s51, 0x18000
	v_lshl_add_u64 v[18:19], v[18:19], 0, s[18:19]
	s_waitcnt vmcnt(2)
	s_barrier
	global_load_lds_dwordx4 v[18:19], off
	v_lshl_add_u64 v[16:17], v[16:17], 0, s[18:19]
	s_add_i32 m0, s51, 0x1a000
	s_add_i32 s60, s51, 0x8000
	s_add_i32 s61, s51, 0xa000
	global_load_lds_dwordx4 v[16:17], off
	v_lshl_add_u64 v[12:13], v[12:13], 0, s[18:19]
	s_mov_b32 m0, s60
	s_add_u32 s22, s66, 0x8080
	global_load_lds_dwordx4 v[12:13], off
	v_lshl_add_u64 v[12:13], v[14:15], 0, s[18:19]
	s_mov_b32 m0, s61
	s_addc_u32 s23, s67, 0
	global_load_lds_dwordx4 v[12:13], off
	s_add_i32 m0, s51, 0x1c000
	v_lshl_add_u64 v[12:13], s[22:23], 0, v[140:141]
	global_load_lds_dwordx4 v[12:13], off
	s_add_i32 m0, s51, 0x1e000
	v_lshl_add_u64 v[12:13], s[22:23], 0, v[144:145]
	s_add_u32 s22, s64, 0x20080
	s_addc_u32 s23, s65, 0
	s_add_i32 s63, s51, 0xc000
	global_load_lds_dwordx4 v[12:13], off
	v_lshl_add_u64 v[12:13], s[22:23], 0, v[138:139]
	s_mov_b32 m0, s63
	s_add_i32 s69, s51, 0xe000
	global_load_lds_dwordx4 v[12:13], off
	v_lshl_add_u64 v[12:13], s[22:23], 0, v[142:143]
	s_mov_b32 m0, s69
	v_readlane_b32 s22, v254, 17
	global_load_lds_dwordx4 v[12:13], off
	v_and_b32_e32 v12, 15, v10
	v_and_b32_e32 v13, 48, v10
	v_lshlrev_b32_e32 v12, 6, v12
	v_lshlrev_b32_e32 v15, 2, v10
	v_readlane_b32 s23, v254, 18
	s_add_u32 s10, s10, s22
	v_or_b32_e32 v14, v12, v13
	v_and_b32_e32 v15, 32, v15
	s_addc_u32 s11, s11, s23
	v_bitop3_b32 v12, v12, v15, v13 bitop3:0x36
	v_bitop3_b32 v13, v14, s9, v15 bitop3:0xde
	v_lshl_add_u64 v[10:11], v[10:11], 4, s[10:11]
	s_mov_b32 s9, 0x72600000
	s_mov_b32 s10, s8
	s_mov_b32 s11, s8
	v_add_co_u32_e32 v10, vcc, s9, v10
	s_mov_b32 s9, s8
	v_mov_b64_e32 v[16:17], s[10:11]
	v_addc_co_u32_e32 v11, vcc, 0, v11, vcc
	v_mov_b64_e32 v[14:15], s[8:9]
	s_cmpk_lt_u32 s20, 0x100
	v_or_b32_e32 v160, s21, v12
	global_store_dwordx4 v[10:11], v[14:17], off
	global_store_dwordx4 v[10:11], v[14:17], off
	global_store_dwordx4 v[10:11], v[14:17], off
	global_store_dwordx4 v[10:11], v[14:17], off
	global_store_dwordx4 v[10:11], v[14:17], off
	global_store_dwordx4 v[10:11], v[14:17], off
	global_store_dwordx4 v[10:11], v[14:17], off
	global_store_dwordx4 v[10:11], v[14:17], off
	s_cselect_b64 s[20:21], -1, 0
	s_ashr_i32 s72, s95, 31
	s_waitcnt vmcnt(16)
	s_add_u32 s22, s2, s95
	s_addc_u32 s23, s96, s72
	s_add_i32 s73, 0, 0x10000
	s_add_i32 s74, 0, 0x14000
	v_add_u32_e32 v161, 0, v13
	v_mov_b64_e32 v[148:149], s[24:25]
	v_add_u32_e32 v162, s73, v160
	v_add_u32_e32 v163, s74, v160
	s_mov_b64 s[24:25], 0x100
	s_mov_b64 s[26:27], 0x180
	s_mov_b64 s[28:29], 0x200
	s_mov_b64 s[30:31], 0x280
	s_mov_b64 s[34:35], 0x300
	s_mov_b64 s[36:37], 0x380
	s_mov_b32 s38, 0x3cd083aa
	s_mov_b32 s75, 0xc3e00000
	v_mov_b32_e32 v164, 0x43e00000
	s_barrier
	s_branch .LBB0_3419

.LBB0_3569:
	s_add_u32 s56, s16, 0x4fc00000
	s_addc_u32 s57, s17, 0
	s_add_u32 s64, s16, 0x5fc00000
	s_addc_u32 s65, s17, 0
	s_add_u32 s66, s16, 0x26c00000
	s_addc_u32 s67, s17, 0
	s_add_u32 s68, s16, 0x72000000
	s_mov_b64 s[14:15], 0x80
	s_addc_u32 s69, s17, 0
	s_lshl_b32 s10, s10, 12
	s_add_i32 m0, s35, 0x18000
	v_lshl_add_u64 v[26:27], v[26:27], 0, s[14:15]
	s_lshl_b32 s9, s9, 13
	s_and_b32 s19, s10, 0x3000
	s_waitcnt vmcnt(2)
	s_barrier
	global_load_lds_dwordx4 v[26:27], off
	v_lshl_add_u64 v[24:25], v[24:25], 0, s[14:15]
	s_add_i32 m0, s35, 0x1a000
	s_add_i32 s71, s35, 0x8000
	s_add_i32 s72, s35, 0xa000
	global_load_lds_dwordx4 v[24:25], off
	v_lshl_add_u64 v[20:21], v[20:21], 0, s[14:15]
	s_mov_b32 m0, s71
	s_add_u32 s10, s60, 0x8080
	global_load_lds_dwordx4 v[20:21], off
	v_lshl_add_u64 v[20:21], v[22:23], 0, s[14:15]
	s_mov_b32 m0, s72
	s_addc_u32 s11, s61, 0
	global_load_lds_dwordx4 v[20:21], off
	s_add_i32 m0, s35, 0x1c000
	v_lshl_add_u64 v[20:21], s[10:11], 0, v[148:149]
	global_load_lds_dwordx4 v[20:21], off
	s_add_i32 m0, s35, 0x1e000
	v_lshl_add_u64 v[20:21], s[10:11], 0, v[152:153]
	s_add_u32 s10, s6, 0x20080
	s_addc_u32 s11, s7, 0
	s_add_i32 s73, s35, 0xc000
	global_load_lds_dwordx4 v[20:21], off
	v_lshl_add_u64 v[20:21], s[10:11], 0, v[146:147]
	s_mov_b32 m0, s73
	s_add_i32 s74, s35, 0xe000
	global_load_lds_dwordx4 v[20:21], off
	v_lshl_add_u64 v[20:21], s[10:11], 0, v[150:151]
	s_mov_b32 m0, s74
	v_and_b32_e32 v1, 15, v18
	global_load_lds_dwordx4 v[20:21], off
	v_readlane_b32 s10, v254, 17
	v_and_b32_e32 v20, 48, v18
	v_lshlrev_b32_e32 v1, 6, v1
	v_lshlrev_b32_e32 v22, 2, v18
	v_readlane_b32 s11, v254, 18
	s_add_u32 s10, s16, s10
	v_or_b32_e32 v21, v1, v20
	v_and_b32_e32 v22, 32, v22
	s_addc_u32 s11, s17, s11
	v_bitop3_b32 v1, v1, v22, v20 bitop3:0x36
	v_bitop3_b32 v20, v21, s9, v22 bitop3:0xde
	v_lshl_add_u64 v[18:19], v[18:19], 4, s[10:11]
	s_mov_b32 s9, 0x72600000
	s_mov_b32 s10, s8
	s_mov_b32 s11, s8
	v_add_co_u32_e32 v18, vcc, s9, v18
	s_mov_b32 s9, s8
	v_mov_b64_e32 v[24:25], s[10:11]
	v_addc_co_u32_e32 v19, vcc, 0, v19, vcc
	v_mov_b64_e32 v[22:23], s[8:9]
	global_store_dwordx4 v[18:19], v[22:25], off
	global_store_dwordx4 v[18:19], v[22:25], off
	global_store_dwordx4 v[18:19], v[22:25], off
	global_store_dwordx4 v[18:19], v[22:25], off
	global_store_dwordx4 v[18:19], v[22:25], off
	global_store_dwordx4 v[18:19], v[22:25], off
	global_store_dwordx4 v[18:19], v[22:25], off
	global_store_dwordx4 v[18:19], v[22:25], off
	global_store_dwordx4 v[18:19], v[22:25], off
	global_store_dwordx4 v[18:19], v[22:25], off
	global_store_dwordx4 v[18:19], v[22:25], off
	global_store_dwordx4 v[18:19], v[22:25], off
	global_store_dwordx4 v[18:19], v[22:25], off
	global_store_dwordx4 v[18:19], v[22:25], off
	global_store_dwordx4 v[18:19], v[22:25], off
	global_store_dwordx4 v[18:19], v[22:25], off
	global_store_dwordx4 v[18:19], v[22:25], off
	global_store_dwordx4 v[18:19], v[22:25], off
	s_cmpk_lt_u32 s18, 0x100
	s_waitcnt vmcnt(26)
	s_cselect_b64 s[10:11], -1, 0
	s_ashr_i32 s75, s95, 31
	s_add_u32 s16, s2, s95
	v_or_b32_e32 v1, s19, v1
	v_add_u32_e32 v176, 0, v20
	s_addc_u32 s17, s96, s75
	s_add_i32 s76, 0, 0x10000
	s_add_i32 s77, 0, 0x14000
	s_mov_b64 s[18:19], 0x100
	s_mov_b64 s[20:21], 0x180
	s_mov_b64 s[22:23], 0x200
	s_mov_b64 s[24:25], 0x280
	s_mov_b64 s[26:27], 0x300
	s_mov_b64 s[28:29], 0x380
	s_mov_b32 s30, 0x3d800000
	s_mov_b32 s34, 0xbfb8aa3b
	s_mov_b32 s36, 0x3e000000
	s_movk_i32 s78, 0x1000
	v_mov_b64_e32 v[156:157], 0x400
	v_mov_b64_e32 v[158:159], 0x3ff
	s_barrier
	s_branch .LBB0_3572
